# attention: V^T LDS tile key-permuted so each PV B-fragment is one 128-bit LDS read (was two 64-bit halves)
# baseline (speedup 1.0000x reference)
; __device__ __forceinline__ void phase_attention(const Frame& F, const Args& a) {
;     constexpr int ABUF = 35840;
;     const bf16_t* QK = (const bf16_t*)(F.ws + WS_Z); const bf16_t* VT = (const bf16_t*)(F.ws + WS_YTL); bf16_t* O = (bf16_t*)(F.ws + WS_MIX);
;     const int fr = F.lane & 15, fq = F.lane >> 4;
;     const int key0 = F.tid >> 4, c16 = F.tid & 15, dim0 = F.tid >> 3, c8 = F.tid & 7;
;     for (int unit = ((F.G % 8 == 0) ? (F.bid % 8) * (F.G / 8) + F.bid / 8 : F.bid); unit < 256; unit += F.G) {
;         const int b = unit >> 7, h = (unit >> 5) & 3, n = unit & 31;
;         const int kt_lo = (2 * n - 2) < 0 ? 0 : (2 * n - 2), kt_hi = (2 * n + 3) > 63 ? 63 : (2 * n + 3), nband = kt_hi - kt_lo + 1, ntile = nband + 4, nstep = 2 * ntile;
;         u32x4 kreg[2], vreg[2];
;         const bf16_t* kbase = QK + 2048 + h * 128 + 8 * c16; const bf16_t* vbase = VT + (size_t)(h * 128 + dim0) * T0 + 8 * c8;
.LBB0_2767:
	s_cmp_lt_i32 s94, 14
	s_cselect_b64 s[0:1], -1, 0
	s_and_b64 s[4:5], s[0:1], s[4:5]
	s_andn2_b64 vcc, exec, s[4:5]
	s_cbranch_vccnz .LBB0_2792
	v_readlane_b32 s0, v254, 0
	v_readlane_b32 s1, v254, 1
	s_mov_b32 s2, s0
	s_ashr_i32 s1, s2, 3
	s_ashr_i32 s2, s3, 31
	s_lshr_b32 s2, s2, 29
	s_add_i32 s2, s3, s2
	s_and_b32 s6, s2, -8
	s_sub_i32 s6, s3, s6
	s_mul_i32 s1, s1, s6
	s_ashr_i32 s2, s2, 3
	s_and_b32 s0, s0, 7
	s_add_i32 s1, s1, s2
	s_cmp_eq_u32 s0, 0
	s_cselect_b32 s18, s1, s3
	s_cmpk_gt_i32 s18, 0xff
	s_mov_b32 s7, 0
	s_cbranch_scc1 .LBB0_2792
	v_lshlrev_b32_e32 v6, 3, v0
	v_and_b32_e32 v2, 0x78, v6
	v_lshlrev_b32_e32 v150, 1, v2
	v_mov_b32_e32 v2, 0
	v_mov_b32_e32 v151, v2
	v_lshl_add_u64 v[4:5], s[92:93], 0, v[150:151]
	s_mov_b64 s[0:1], 0x3a601000
	v_lshl_add_u64 v[152:153], v[4:5], 0, s[0:1]
	v_and_b32_e32 v4, 56, v6
	v_lshlrev_b32_e32 v154, 1, v4
	v_mov_b32_e32 v155, v2
	v_lshl_add_u64 v[4:5], s[92:93], 0, v[154:155]
	s_mov_b64 s[0:1], 0x3d900000
	v_lshl_add_u64 v[156:157], v[4:5], 0, s[0:1]
	v_and_b32_e32 v4, 48, v1
	v_mov_b32_e32 v5, v2
	v_lshrrev_b32_e32 v3, 4, v1
	v_lshl_add_u64 v[4:5], s[92:93], 0, v[4:5]
	s_mov_b64 s[0:1], 0x3a600000
	v_lshl_add_u64 v[158:159], v[4:5], 0, s[0:1]
	v_lshlrev_b32_e32 v4, 2, v3
	v_mov_b32_e32 v5, v2
	v_and_b32_e32 v172, 15, v0
	v_lshrrev_b32_e32 v173, 4, v0
	v_lshrrev_b32_e32 v174, 3, v0
	v_lshl_add_u64 v[6:7], s[92:93], 0, v[4:5]
	s_mov_b64 s[0:1], 0x41b00000
	v_mul_u32_u24_e32 v8, 0x88, v173
	v_mul_u32_u24_e32 v9, 0x48, v174
	v_lshlrev_b32_e32 v151, 4, v3
	v_lshl_add_u64 v[160:161], v[6:7], 0, s[0:1]
	v_sub_u32_e32 v3, v4, v172
	v_readlane_b32 s0, v254, 2
	v_lshlrev_b32_e32 v177, 1, v8
	v_lshlrev_b32_e32 v179, 1, v9
	v_add_u32_e32 v181, 0xffffff7f, v3
	s_lshr_b32 s19, s0, 8
	s_lshl_b32 s0, s74, 5
	v_mbcnt_lo_u32_b32 v3, -1, 0
	v_and_b32_e32 v155, 48, v0
	v_mul_u32_u24_e32 v175, 0x110, v172
	v_mul_u32_u24_e32 v176, 0x90, v172
	v_add3_u32 v178, 0, v177, v150
	v_add3_u32 v180, 0, v179, v154
	v_and_b32_e32 v224, 4, v0
	v_lshlrev_b32_e32 v224, 4, v224
	v_and_b32_e32 v225, 1, v0
	v_lshl_or_b32 v224, v225, 5, v224
	v_and_b32_e32 v225, 2, v0
	v_lshl_or_b32 v224, v225, 2, v224
	v_add_u32_e32 v225, v179, v224
	v_add_u32_e32 v226, 0x4400, v225
	v_add_u32_e32 v227, 0x6800, v225
	s_and_b32 s20, s0, 0x60
	s_movk_i32 s21, 0x1400
	s_mov_b64 s[8:9], 0x110000
	s_movk_i32 s22, 0xfeff
	s_mov_b32 s23, 0xff800000
	s_movk_i32 s24, 0xfefe
	s_mov_b32 s25, 0x41800000
	s_mov_b32 s26, 0xc3e00000
	v_mbcnt_hi_u32_b32 v182, -1, v3
	v_mov_b32_e32 v183, 0xff800000
	v_mov_b32_e32 v184, 0x43e00000
	s_branch .LBB0_2772

; __device__ __forceinline__ void phase_attention(const Frame& F, const Args& a) {
;     ...
;         u32x4 kreg[2], vreg[2];
;         const bf16_t* kbase = QK + 2048 + h * 128 + 8 * c16; const bf16_t* vbase = VT + (size_t)(h * 128 + dim0) * T0 + 8 * c8;
;     ...
;         __syncthreads();
;         ATT_LOAD(0); ATT_STORE(0);
;         __syncthreads();
.LBB0_2776:
	s_bfe_u32 s10, s18, 0x20005
	s_lshl_b32 s1, s10, 7
	v_or_b32_e32 v3, s1, v174
	v_mul_u32_u24_e32 v66, 0x4400, v3
	s_lshl_b32 s6, s1, 1
	v_mov_b32_e32 v67, v2
	v_lshl_add_u64 v[162:163], v[152:153], 0, s[6:7]
	v_lshl_add_u64 v[164:165], v[156:157], 0, v[66:67]
	v_add_u32_e32 v3, s0, v173
	s_ashr_i32 s1, s0, 31
	v_mad_i64_i32 v[66:67], s[16:17], v3, s21, v[162:163]
	v_add_u32_e32 v3, 32, v3
	s_lshl_b64 s[0:1], s[0:1], 1
	v_lshl_add_u64 v[166:167], v[164:165], 0, s[8:9]
	v_mad_i64_i32 v[74:75], s[16:17], v3, s21, v[162:163]
	v_lshl_add_u64 v[78:79], v[164:165], 0, s[0:1]
	v_lshl_add_u64 v[82:83], v[166:167], 0, s[0:1]
	global_load_dwordx4 v[66:69], v[66:67], off
	s_nop 0
	global_load_dwordx4 v[74:77], v[74:75], off
	s_nop 0
	global_load_dwordx4 v[78:81], v[78:79], off
	s_nop 0
	global_load_dwordx4 v[82:85], v[82:83], off
	s_cmp_lt_i32 s27, -4
	s_waitcnt vmcnt(3)
	ds_write_b128 v178, v[66:69]
	s_waitcnt vmcnt(2)
	ds_write_b128 v178, v[74:77] offset:8704
	s_waitcnt vmcnt(1)
	ds_write2_b64 v226, v[78:79], v[80:81] offset1:2
	s_waitcnt vmcnt(0)
	ds_write2_b64 v227, v[82:83], v[84:85] offset1:2
	s_waitcnt lgkmcnt(0)
	s_barrier
	s_cbranch_scc1 .LBB0_2771
	v_and_b32_e32 v5, 64, v182
	v_xor_b32_e32 v3, 16, v182
	v_add_u32_e32 v5, 64, v5
	v_cmp_lt_i32_e32 vcc, v3, v5
	s_add_i32 s11, s27, 5
	s_sub_i32 s33, -5, s27
	v_cndmask_b32_e32 v3, v182, v3, vcc
	v_lshlrev_b32_e32 v185, 2, v3
	v_xor_b32_e32 v3, 32, v182
	v_cmp_lt_i32_e32 vcc, v3, v5
	s_max_i32 s34, s11, s33
	s_lshl_b32 s29, s14, 12
	v_cndmask_b32_e32 v3, v182, v3, vcc
	v_lshlrev_b32_e32 v186, 2, v3
	v_cvt_f32_u32_e32 v3, s34
	s_lshl_b32 s0, s13, 7
	s_bitset1_b32 s29, 9
	s_or_b32 s35, s0, s20
	v_rcp_iflag_f32_e32 v3, v3
	s_add_i32 s36, s29, s35
	v_or_b32_e32 v5, s36, v172
	v_mad_i64_i32 v[168:169], s[0:1], v5, s21, 0
	v_mul_f32_e32 v3, 0x4f7ffffe, v3
	v_cvt_u32_f32_e32 v3, v3
	v_or_b32_e32 v5, 16, v5
	v_mad_i64_i32 v[170:171], s[0:1], v5, s21, 0
	s_sub_i32 s0, 0, s34
	v_readfirstlane_b32 s1, v3
	s_mul_i32 s0, s0, s1
	s_lshl_b32 s31, s10, 2
	s_mul_hi_u32 s0, s1, s0
	s_sub_i32 s39, s2, s12
	s_lshl_b32 s6, s11, 1
	s_lshl_b32 s30, s14, 8
	s_mov_b32 s10, 0
	s_add_i32 s31, s31, s19
	s_ashr_i32 s37, s11, 31
	s_add_i32 s38, s1, s0
	s_add_i32 s39, s39, -4
	s_mov_b32 s41, 0
	s_mov_b32 s11, 0
	s_mov_b32 s42, 0

; __device__ __forceinline__ void phase_attention(const Frame& F, const Args& a) {
;     ...
;                 float mx = s[m][0][0];
; #pragma unroll
;                 for (int nn = 0; nn < 4; ++nn)
; #pragma unroll
;                     for (int j = 0; j < 4; ++j) mx = fmaxf(mx, s[m][nn][j]);
;                 mx = fmaxf(mx, __shfl_xor(mx, 16)); mx = fmaxf(mx, __shfl_xor(mx, 32));
;                 const float mnew = fmaxf(mrun[m], mx), alpha = __expf(mrun[m] - mnew); mrun[m] = mnew;
;                 float rs = 0.f;
; #pragma unroll
;                 for (int nn = 0; nn < 4; ++nn)
; #pragma unroll
;                     for (int j = 0; j < 4; ++j) { const float p = __expf(s[m][nn][j] - mnew); s[m][nn][j] = p; rs += p; }
;                 rs += __shfl_xor(rs, 16); rs += __shfl_xor(rs, 32);
;                 lrun[m] = lrun[m] * alpha + rs;
; #pragma unroll
;                 for (int nd = 0; nd < 8; ++nd) o[m][nd] = o[m][nd] * alpha;
.LBB0_2786:
	s_waitcnt lgkmcnt(0)
	v_add_f32_e32 v5, v142, v143
	v_max_f32_e32 v142, v139, v139
	v_max_f32_e32 v143, v138, v138
	v_max_f32_e32 v142, v143, v142
	v_max3_f32 v142, v142, v140, v141
	v_max3_f32 v142, v142, v134, v135
	v_max3_f32 v142, v142, v136, v137
	v_max3_f32 v142, v142, v130, v131
	v_max3_f32 v142, v142, v132, v133
	v_max3_f32 v142, v142, v122, v123
	v_max3_f32 v142, v142, v124, v125
	ds_bpermute_b32 v143, v185, v142
	v_sub_f32_e32 v4, v4, v3
	v_mul_f32_e32 v4, 0x3fb8aa3b, v4
	v_exp_f32_e32 v4, v4
	s_add_i32 s0, s39, s42
	s_waitcnt lgkmcnt(0)
	v_max_f32_e32 v143, v143, v143
	v_max_f32_e32 v142, v142, v143
	ds_bpermute_b32 v143, v186, v142
	v_fmac_f32_e32 v5, v189, v4
	v_pk_mul_f32 v[116:117], v[116:117], v[4:5] op_sel_hi:[1,0]
	v_pk_mul_f32 v[114:115], v[114:115], v[4:5] op_sel_hi:[1,0]
	v_pk_mul_f32 v[112:113], v[112:113], v[4:5] op_sel_hi:[1,0]
	s_waitcnt lgkmcnt(0)
	v_max3_f32 v142, v187, v142, v143
	v_sub_f32_e32 v138, v138, v142
	v_mul_f32_e32 v138, 0x3fb8aa3b, v138
	v_sub_f32_e32 v139, v139, v142
	v_exp_f32_e32 v138, v138
	v_mul_f32_e32 v139, 0x3fb8aa3b, v139
	v_sub_f32_e32 v140, v140, v142
	v_exp_f32_e32 v139, v139
	v_mul_f32_e32 v140, 0x3fb8aa3b, v140
	v_sub_f32_e32 v141, v141, v142
	v_exp_f32_e32 v140, v140
	v_mul_f32_e32 v141, 0x3fb8aa3b, v141
	v_sub_f32_e32 v134, v134, v142
	v_exp_f32_e32 v141, v141
	v_mul_f32_e32 v134, 0x3fb8aa3b, v134
	v_sub_f32_e32 v135, v135, v142
	v_add_f32_e32 v143, 0, v138
	v_exp_f32_e32 v134, v134
	v_mul_f32_e32 v135, 0x3fb8aa3b, v135
	v_sub_f32_e32 v136, v136, v142
	v_sub_f32_e32 v130, v130, v142
	v_add_f32_e32 v143, v139, v143
	v_exp_f32_e32 v135, v135
	v_mul_f32_e32 v136, 0x3fb8aa3b, v136
	v_sub_f32_e32 v137, v137, v142
	v_mul_f32_e32 v130, 0x3fb8aa3b, v130
	v_add_f32_e32 v143, v140, v143
	v_exp_f32_e32 v136, v136
	v_mul_f32_e32 v137, 0x3fb8aa3b, v137
	v_exp_f32_e32 v144, v130
	v_sub_f32_e32 v130, v131, v142
	v_add_f32_e32 v143, v141, v143
	v_exp_f32_e32 v137, v137
	v_mul_f32_e32 v130, 0x3fb8aa3b, v130
	v_add_f32_e32 v143, v134, v143
	v_exp_f32_e32 v145, v130
	v_sub_f32_e32 v130, v132, v142
	v_add_f32_e32 v143, v135, v143
	v_mul_f32_e32 v130, 0x3fb8aa3b, v130
	v_add_f32_e32 v143, v136, v143
	v_exp_f32_e32 v146, v130
	v_sub_f32_e32 v130, v133, v142
	v_sub_f32_e32 v122, v122, v142
	v_add_f32_e32 v143, v137, v143
	v_mul_f32_e32 v130, 0x3fb8aa3b, v130
	v_mul_f32_e32 v122, 0x3fb8aa3b, v122
	v_exp_f32_e32 v147, v130
	v_add_f32_e32 v130, v144, v143
	v_exp_f32_e32 v143, v122
	v_sub_f32_e32 v122, v123, v142
	v_mul_f32_e32 v122, 0x3fb8aa3b, v122
	v_exp_f32_e32 v123, v122
	v_sub_f32_e32 v122, v124, v142
	v_mul_f32_e32 v122, 0x3fb8aa3b, v122
	v_add_f32_e32 v130, v145, v130
	v_exp_f32_e32 v124, v122
	v_sub_f32_e32 v122, v125, v142
	v_add_f32_e32 v130, v146, v130
	v_mul_f32_e32 v122, 0x3fb8aa3b, v122
	v_add_f32_e32 v130, v147, v130
	v_exp_f32_e32 v125, v122
	v_add_f32_e32 v122, v143, v130
	v_add_f32_e32 v122, v123, v122
	v_add_f32_e32 v122, v124, v122
	v_add_f32_e32 v122, v125, v122
	ds_bpermute_b32 v130, v185, v122
	v_pk_mul_f32 v[110:111], v[110:111], v[4:5] op_sel_hi:[1,0]
	v_pk_mul_f32 v[96:97], v[96:97], v[4:5] op_sel_hi:[1,0]
	v_pk_mul_f32 v[94:95], v[94:95], v[4:5] op_sel_hi:[1,0]
	v_pk_mul_f32 v[100:101], v[100:101], v[4:5] op_sel_hi:[1,0]
	s_waitcnt lgkmcnt(0)
	v_add_f32_e32 v122, v122, v130
	v_pk_mul_f32 v[98:99], v[98:99], v[4:5] op_sel_hi:[1,0]
	v_pk_mul_f32 v[104:105], v[104:105], v[4:5] op_sel_hi:[1,0]
	v_pk_mul_f32 v[102:103], v[102:103], v[4:5] op_sel_hi:[1,0]
	v_pk_mul_f32 v[108:109], v[108:109], v[4:5] op_sel_hi:[1,0]
	v_pk_mul_f32 v[106:107], v[106:107], v[4:5] op_sel_hi:[1,0]
	v_pk_mul_f32 v[88:89], v[88:89], v[4:5] op_sel_hi:[1,0]
	v_pk_mul_f32 v[86:87], v[86:87], v[4:5] op_sel_hi:[1,0]
	v_pk_mul_f32 v[92:93], v[92:93], v[4:5] op_sel_hi:[1,0]
	v_pk_mul_f32 v[90:91], v[90:91], v[4:5] op_sel_hi:[1,0]
	v_sub_f32_e32 v4, v187, v142
	ds_bpermute_b32 v130, v186, v122
	v_mul_f32_e32 v4, 0x3fb8aa3b, v4
	v_exp_f32_e32 v4, v4
	s_add_i32 s0, s0, s43
	s_waitcnt lgkmcnt(0)
; #define GAS __attribute__((address_space(1)))
; #define LAS __attribute__((address_space(3)))
; __device__ __forceinline__ unsigned pk4_fp8(float a, float b, float c, float d) { int w = 0; w = __builtin_amdgcn_cvt_pk_fp8_f32(sat8(a), sat8(b), w, false); w = __builtin_amdgcn_cvt_pk_fp8_f32(sat8(c), sat8(d), w, true); return (unsigned)w; }
; __device__ __forceinline__ unsigned cvt_pk_bf16(float lo, float hi) { unsigned r; asm volatile("v_cvt_pk_bf16_f32 %0, %1, %2" : "=v"(r) : "v"(lo), "v"(hi)); return r; }
; __device__ __forceinline__ void phase_attention(const Frame& F, const Args& a) {
;     ...
;                 for (int ks = 0; ks < 2; ++ks) { u32x4 w; w.x = cvt_pk_bf16(s[m][2 * ks][0], s[m][2 * ks][1]); w.y = cvt_pk_bf16(s[m][2 * ks][2], s[m][2 * ks][3]);
;                     w.z = cvt_pk_bf16(s[m][2 * ks + 1][0], s[m][2 * ks + 1][1]); w.w = cvt_pk_bf16(s[m][2 * ks + 1][2], s[m][2 * ks + 1][3]); pf[m][ks] = __builtin_bit_cast(bf16x8, w); }
;             }
;             __builtin_amdgcn_s_setprio(1);
; #pragma unroll
;             for (int ks = 0; ks < 2; ++ks)
; #pragma unroll
;                 for (int nd = 0; nd < 8; ++nd) { const LAS bf16_t* vp = Vs + (16 * nd + fr) * 72 + 32 * ks + 4 * fq;
;                     u32x4 w; const u32x2 lo = *(const LAS u32x2*)vp, hi = *(const LAS u32x2*)(vp + 16); w.x = lo.x; w.y = lo.y; w.z = hi.x; w.w = hi.y;
;                     const bf16x8 vf = __builtin_bit_cast(bf16x8, w);
; #pragma unroll
;                     for (int m = 0; m < 2; ++m) o[m][nd] = __builtin_amdgcn_mfma_f32_16x16x32_bf16(vf, pf[m][ks], o[m][nd], 0, 0, 0); }
;             __builtin_amdgcn_s_setprio(0);
;             if (ti == ntile - 1) {
; #pragma unroll
;                 for (int m = 0; m < 2; ++m) { const float inv = 16.0f / lrun[m]; unsigned char* op = (unsigned char*)O + (size_t)(qrow + 16 * m + fr) * D + qh * 128 + 4 * fq;
; #pragma unroll
;                     for (int nd = 0; nd < 8; ++nd) { const f32x4 v = o[m][nd] * inv; *(GAS unsigned*)(op + 16 * nd) = pk4_fp8(v[0], v[1], v[2], v[3]); } }
;             }
;             if (step + 1 < nstep) ATT_STORE((step + 1) & 1);
	v_add_f32_e32 v122, v122, v130
	v_fmac_f32_e32 v122, v188, v4
	v_pk_mul_f32 v[72:73], v[72:73], v[4:5] op_sel_hi:[1,0]
	v_pk_mul_f32 v[70:71], v[70:71], v[4:5] op_sel_hi:[1,0]
	v_pk_mul_f32 v[64:65], v[64:65], v[4:5] op_sel_hi:[1,0]
	v_pk_mul_f32 v[62:63], v[62:63], v[4:5] op_sel_hi:[1,0]
	v_pk_mul_f32 v[60:61], v[60:61], v[4:5] op_sel_hi:[1,0]
	v_pk_mul_f32 v[58:59], v[58:59], v[4:5] op_sel_hi:[1,0]
	v_pk_mul_f32 v[56:57], v[56:57], v[4:5] op_sel_hi:[1,0]
	v_pk_mul_f32 v[54:55], v[54:55], v[4:5] op_sel_hi:[1,0]
	v_pk_mul_f32 v[52:53], v[52:53], v[4:5] op_sel_hi:[1,0]
	v_pk_mul_f32 v[50:51], v[50:51], v[4:5] op_sel_hi:[1,0]
	v_pk_mul_f32 v[48:49], v[48:49], v[4:5] op_sel_hi:[1,0]
	v_pk_mul_f32 v[46:47], v[46:47], v[4:5] op_sel_hi:[1,0]
	v_pk_mul_f32 v[44:45], v[44:45], v[4:5] op_sel_hi:[1,0]
	v_pk_mul_f32 v[42:43], v[42:43], v[4:5] op_sel_hi:[1,0]
	v_pk_mul_f32 v[40:41], v[40:41], v[4:5] op_sel_hi:[1,0]
	v_pk_mul_f32 v[38:39], v[38:39], v[4:5] op_sel_hi:[1,0]
	v_cvt_pk_bf16_f32 v130, v138, v139
	v_cvt_pk_bf16_f32 v131, v140, v141
	v_cvt_pk_bf16_f32 v132, v134, v135
	v_cvt_pk_bf16_f32 v133, v136, v137
	v_cvt_pk_bf16_f32 v134, v144, v145
	v_cvt_pk_bf16_f32 v135, v146, v147
	v_cvt_pk_bf16_f32 v136, v143, v123
	v_cvt_pk_bf16_f32 v137, v124, v125
	s_setprio 1
	v_add3_u32 v4, s44, v151, v176
	v_add_u32_e32 v123, 0x4000, v4
	ds_read_b128 v[138:141], v123 offset:1024
	v_add_u32_e32 v143, 0x4800, v4
	v_add_u32_e32 v144, 0x5000, v4
	v_add_u32_e32 v145, 0x5800, v4
	v_add_u32_e32 v146, 0x6800, v4
	v_add_u32_e32 v147, 0x7000, v4
	v_add_u32_e32 v148, 0x7800, v4
	v_add_u32_e32 v4, 0x8000, v4
	s_waitcnt lgkmcnt(0)
	v_mfma_f32_16x16x32_bf16 v[114:117], v[138:141], v[126:129], v[114:117]
	v_mfma_f32_16x16x32_bf16 v[70:73], v[138:141], v[130:133], v[70:73]
	ds_read_b128 v[138:141], v143 offset:1280
	s_waitcnt lgkmcnt(0)
	v_mfma_f32_16x16x32_bf16 v[110:113], v[138:141], v[126:129], v[110:113]
	v_mfma_f32_16x16x32_bf16 v[62:65], v[138:141], v[130:133], v[62:65]
	ds_read_b128 v[138:141], v144 offset:1536
	s_waitcnt lgkmcnt(0)
	v_mfma_f32_16x16x32_bf16 v[94:97], v[138:141], v[126:129], v[94:97]
	v_mfma_f32_16x16x32_bf16 v[58:61], v[138:141], v[130:133], v[58:61]
	ds_read_b128 v[138:141], v145 offset:1792
	s_waitcnt lgkmcnt(0)
	v_mfma_f32_16x16x32_bf16 v[98:101], v[138:141], v[126:129], v[98:101]
	v_mfma_f32_16x16x32_bf16 v[54:57], v[138:141], v[130:133], v[54:57]
	ds_read_b128 v[138:141], v146
	s_waitcnt lgkmcnt(0)
	v_mfma_f32_16x16x32_bf16 v[102:105], v[138:141], v[126:129], v[102:105]
	v_mfma_f32_16x16x32_bf16 v[50:53], v[138:141], v[130:133], v[50:53]
	ds_read_b128 v[138:141], v147 offset:256
	s_waitcnt lgkmcnt(0)
	v_mfma_f32_16x16x32_bf16 v[106:109], v[138:141], v[126:129], v[106:109]
	v_mfma_f32_16x16x32_bf16 v[46:49], v[138:141], v[130:133], v[46:49]
	ds_read_b128 v[138:141], v148 offset:512
	s_waitcnt lgkmcnt(0)
	v_mfma_f32_16x16x32_bf16 v[86:89], v[138:141], v[126:129], v[86:89]
	v_mfma_f32_16x16x32_bf16 v[42:45], v[138:141], v[130:133], v[42:45]
	ds_read_b128 v[138:141], v4 offset:768
	s_waitcnt lgkmcnt(0)
	v_mfma_f32_16x16x32_bf16 v[90:93], v[138:141], v[126:129], v[90:93]
	ds_read_b128 v[124:127], v123 offset:1088
	s_waitcnt lgkmcnt(0)
	v_mfma_f32_16x16x32_bf16 v[114:117], v[124:127], v[118:121], v[114:117]
	v_mfma_f32_16x16x32_bf16 v[70:73], v[124:127], v[134:137], v[70:73]
	ds_read_b128 v[124:127], v143 offset:1344
	s_waitcnt lgkmcnt(0)
	v_mfma_f32_16x16x32_bf16 v[110:113], v[124:127], v[118:121], v[110:113]
	v_mfma_f32_16x16x32_bf16 v[62:65], v[124:127], v[134:137], v[62:65]
	ds_read_b128 v[124:127], v144 offset:1600
	s_waitcnt lgkmcnt(0)
	v_mfma_f32_16x16x32_bf16 v[94:97], v[124:127], v[118:121], v[94:97]
	v_mfma_f32_16x16x32_bf16 v[58:61], v[124:127], v[134:137], v[58:61]
	ds_read_b128 v[124:127], v145 offset:1856
	s_waitcnt lgkmcnt(0)
	v_mfma_f32_16x16x32_bf16 v[98:101], v[124:127], v[118:121], v[98:101]
	v_mfma_f32_16x16x32_bf16 v[54:57], v[124:127], v[134:137], v[54:57]
	ds_read_b128 v[124:127], v146 offset:64
	s_waitcnt lgkmcnt(0)
	v_mfma_f32_16x16x32_bf16 v[102:105], v[124:127], v[118:121], v[102:105]
	v_mfma_f32_16x16x32_bf16 v[50:53], v[124:127], v[134:137], v[50:53]
	ds_read_b128 v[124:127], v147 offset:320
	s_waitcnt lgkmcnt(0)
	v_mfma_f32_16x16x32_bf16 v[106:109], v[124:127], v[118:121], v[106:109]
	v_mfma_f32_16x16x32_bf16 v[46:49], v[124:127], v[134:137], v[46:49]
	ds_read_b128 v[124:127], v148 offset:576
	s_waitcnt lgkmcnt(0)
	v_mfma_f32_16x16x32_bf16 v[86:89], v[124:127], v[118:121], v[86:89]
	v_mfma_f32_16x16x32_bf16 v[42:45], v[124:127], v[134:137], v[42:45]
	ds_read_b128 v[124:127], v4 offset:832
	v_mfma_f32_16x16x32_bf16 v[38:41], v[138:141], v[130:133], v[38:41]
	s_waitcnt lgkmcnt(0)
	v_mfma_f32_16x16x32_bf16 v[90:93], v[124:127], v[118:121], v[90:93]
	v_mfma_f32_16x16x32_bf16 v[38:41], v[124:127], v[134:137], v[38:41]
	s_setprio 0
	s_cmp_lg_u32 s0, 0
	s_cbranch_scc0 .LBB0_2791
	s_andn2_b64 vcc, exec, s[14:15]
	s_cbranch_vccnz .LBB0_2789
.LBB0_2788:
	s_bitcmp1_b32 s40, 0
	s_cselect_b32 s0, 0x8c00, 0
	s_add_i32 s0, s0, 0
	v_add3_u32 v4, s0, v177, v150
	ds_write_b128 v4, v[66:69]
	ds_write_b128 v4, v[74:77] offset:8704
	v_add3_u32 v4, s0, v179, v224
	v_add_u32_e32 v228, 0x4400, v4
	v_add_u32_e32 v229, 0x6800, v4
	ds_write2_b64 v228, v[78:79], v[80:81] offset1:2
	ds_write2_b64 v229, v[82:83], v[84:85] offset1:2
